# loader uses packed f32 mul/fma for the decay prefix and scaling, writes the group decay only where the scanner reads it
# baseline (speedup 1.0000x reference)
.Lld_ldone_p1:
	s_waitcnt vmcnt(21)
	s_mov_b32 s88, 0
	v_add_u32_e32 v83, s88, v7
	v_add_u32_e32 v96, s88, v8
	s_mov_b32 s46, 0x3fb8aa3b
	s_mov_b32 s47, 0x3fb8aa3b
	v_lshlrev_b32_e32 v92, 16, v29
	v_and_b32_e32 v93, s89, v29
	ds_write_b64 v96, v[92:93]
	v_lshlrev_b32_e32 v92, 16, v9
	v_and_b32_e32 v93, s89, v9
	v_lshlrev_b32_e32 v94, 16, v13
	v_and_b32_e32 v95, s89, v13
	v_pk_mul_f32 v[84:85], v[92:93], s[46:47]
	ds_write_b64 v83, v[94:95] offset:0
	v_lshlrev_b32_e32 v92, 16, v17
	v_and_b32_e32 v93, s89, v17
	v_exp_f32_e64 v86, -v84
	v_exp_f32_e64 v87, -v85
	v_exp_f32_e32 v90, v84
	v_exp_f32_e32 v91, v85
	v_lshlrev_b32_e32 v94, 16, v21
	v_and_b32_e32 v95, s89, v21
	v_pk_mul_f32 v[92:93], v[92:93], v[90:91]
	v_pk_mul_f32 v[94:95], v[94:95], v[90:91]
	ds_write_b64 v83, v[92:93] offset:8192
	ds_write_b64 v83, v[94:95] offset:24576
	v_lshlrev_b32_e32 v92, 16, v25
	v_and_b32_e32 v93, s89, v25
	v_pk_mul_f32 v[92:93], v[92:93], v[86:87]
	ds_write_b64 v83, v[92:93] offset:32768
	v_lshlrev_b32_e32 v92, 16, v10
	v_and_b32_e32 v93, s89, v10
	v_lshlrev_b32_e32 v94, 16, v14
	v_and_b32_e32 v95, s89, v14
	v_pk_fma_f32 v[84:85], v[92:93], s[46:47], v[84:85]
	v_pk_mul_f32 v[94:95], v[94:95], v[86:87]
	ds_write_b64 v83, v[94:95] offset:256
	v_lshlrev_b32_e32 v92, 16, v18
	v_and_b32_e32 v93, s89, v18
	v_exp_f32_e64 v88, -v84
	v_exp_f32_e64 v89, -v85
	v_exp_f32_e32 v90, v84
	v_exp_f32_e32 v91, v85
	v_lshlrev_b32_e32 v94, 16, v22
	v_and_b32_e32 v95, s89, v22
	v_pk_mul_f32 v[92:93], v[92:93], v[90:91]
	v_pk_mul_f32 v[94:95], v[94:95], v[90:91]
	ds_write_b64 v83, v[92:93] offset:8448
	ds_write_b64 v83, v[94:95] offset:24832
	v_lshlrev_b32_e32 v92, 16, v26
	v_and_b32_e32 v93, s89, v26
	v_pk_mul_f32 v[92:93], v[92:93], v[88:89]
	ds_write_b64 v83, v[92:93] offset:33024
	v_lshlrev_b32_e32 v92, 16, v11
	v_and_b32_e32 v93, s89, v11
	v_lshlrev_b32_e32 v94, 16, v15
	v_and_b32_e32 v95, s89, v15
	v_pk_fma_f32 v[84:85], v[92:93], s[46:47], v[84:85]
	v_pk_mul_f32 v[94:95], v[94:95], v[88:89]
	ds_write_b64 v83, v[94:95] offset:512
	v_lshlrev_b32_e32 v92, 16, v19
	v_and_b32_e32 v93, s89, v19
	v_exp_f32_e64 v86, -v84
	v_exp_f32_e64 v87, -v85
	v_exp_f32_e32 v90, v84
	v_exp_f32_e32 v91, v85
	v_lshlrev_b32_e32 v94, 16, v23
	v_and_b32_e32 v95, s89, v23
	v_pk_mul_f32 v[92:93], v[92:93], v[90:91]
	v_pk_mul_f32 v[94:95], v[94:95], v[90:91]
	ds_write_b64 v83, v[92:93] offset:8704
	ds_write_b64 v83, v[94:95] offset:25088
	v_lshlrev_b32_e32 v92, 16, v27
	v_and_b32_e32 v93, s89, v27
	v_pk_mul_f32 v[92:93], v[92:93], v[86:87]
	ds_write_b64 v83, v[92:93] offset:33280
	v_lshlrev_b32_e32 v92, 16, v12
	v_and_b32_e32 v93, s89, v12
	v_lshlrev_b32_e32 v94, 16, v16
	v_and_b32_e32 v95, s89, v16
	v_pk_fma_f32 v[84:85], v[92:93], s[46:47], v[84:85]
	v_pk_mul_f32 v[94:95], v[94:95], v[86:87]
	ds_write_b64 v83, v[94:95] offset:768
	v_lshlrev_b32_e32 v92, 16, v20
	v_and_b32_e32 v93, s89, v20
	v_exp_f32_e64 v88, -v84
	v_exp_f32_e64 v89, -v85
	v_exp_f32_e32 v90, v84
	v_exp_f32_e32 v91, v85
	v_lshlrev_b32_e32 v94, 16, v24
	v_and_b32_e32 v95, s89, v24
	v_pk_mul_f32 v[92:93], v[92:93], v[90:91]
	v_pk_mul_f32 v[94:95], v[94:95], v[90:91]
	ds_write_b64 v83, v[92:93] offset:8960
	ds_write_b64 v83, v[88:89] offset:17152
	ds_write_b64 v83, v[94:95] offset:25344
	v_lshlrev_b32_e32 v92, 16, v28
	v_and_b32_e32 v93, s89, v28
	ds_write_b64 v83, v[92:93] offset:33536
	s_mov_b32 s8, 2
	s_lshl_b32 s9, s8, 5
	s_lshl_b32 s33, s81, 3
	s_add_i32 s9, s9, s33
	s_lshl_b32 s33, s6, 8
	s_add_i32 s33, s33, 0x8000
	s_lshl_b32 s45, s6, 12
	s_cmp_lt_u32 s8, 8
	s_cselect_b32 s33, s33, s45
	s_cselect_b32 s44, 0, 0x100
	s_movk_i32 s45, 0xff8
	s_cselect_b32 s45, 0xf8, s45
	s_sub_i32 s9, s9, s44
	s_sub_i32 s45, s45, s9
	s_cmp_lg_u32 s50, 0
	s_cselect_b32 s9, s45, s9
	s_add_i32 s33, s33, s9
	s_lshl_b32 s33, s33, 9
	s_cmp_lg_u32 s50, 0
	s_cbranch_scc1 .Lld_bw_p2
	s_add_u32 s0, s82, s33
	s_addc_u32 s1, s83, 0
	global_load_dword v9, v3, s[0:1]
	global_load_dword v10, v3, s[0:1] offset:512
	global_load_dword v11, v3, s[0:1] offset:1024
	global_load_dword v12, v3, s[0:1] offset:1536
	s_add_u32 s0, s62, s33
	s_addc_u32 s1, s63, 0
	global_load_dword v13, v3, s[0:1]
	global_load_dword v14, v3, s[0:1] offset:512
	global_load_dword v15, v3, s[0:1] offset:1024
	global_load_dword v16, v3, s[0:1] offset:1536
	s_add_u32 s0, s70, s33
	s_addc_u32 s1, s71, 0
	global_load_dword v17, v3, s[0:1]
	global_load_dword v18, v3, s[0:1] offset:512
	global_load_dword v19, v3, s[0:1] offset:1024
	global_load_dword v20, v3, s[0:1] offset:1536
	s_add_u32 s0, s72, s33
	s_addc_u32 s1, s73, 0
	global_load_dword v21, v3, s[0:1]
	global_load_dword v22, v3, s[0:1] offset:512
	global_load_dword v23, v3, s[0:1] offset:1024
	global_load_dword v24, v3, s[0:1] offset:1536
	s_add_u32 s0, s74, s33
	s_addc_u32 s1, s75, 0
	global_load_dword v25, v3, s[0:1]
	global_load_dword v26, v3, s[0:1] offset:512
	global_load_dword v27, v3, s[0:1] offset:1024
	global_load_dword v28, v3, s[0:1] offset:1536
	s_add_u32 s0, s84, s33
	s_addc_u32 s1, s85, 0
	global_load_dword v29, v6, s[0:1]
	s_branch .Lld_ldone_p2

.Lld_ldone_p2:
	s_waitcnt vmcnt(21)
	s_mov_b32 s88, 0xa800
	v_add_u32_e32 v83, s88, v7
	v_add_u32_e32 v96, s88, v8
	s_mov_b32 s46, 0x3fb8aa3b
	s_mov_b32 s47, 0x3fb8aa3b
	v_lshlrev_b32_e32 v92, 16, v118
	v_and_b32_e32 v93, s89, v118
	ds_write_b64 v96, v[92:93]
	v_lshlrev_b32_e32 v92, 16, v98
	v_and_b32_e32 v93, s89, v98
	v_lshlrev_b32_e32 v94, 16, v102
	v_and_b32_e32 v95, s89, v102
	v_pk_mul_f32 v[84:85], v[92:93], s[46:47]
	ds_write_b64 v83, v[94:95] offset:0
	v_lshlrev_b32_e32 v92, 16, v106
	v_and_b32_e32 v93, s89, v106
	v_exp_f32_e64 v86, -v84
	v_exp_f32_e64 v87, -v85
	v_exp_f32_e32 v90, v84
	v_exp_f32_e32 v91, v85
	v_lshlrev_b32_e32 v94, 16, v110
	v_and_b32_e32 v95, s89, v110
	v_pk_mul_f32 v[92:93], v[92:93], v[90:91]
	v_pk_mul_f32 v[94:95], v[94:95], v[90:91]
	ds_write_b64 v83, v[92:93] offset:8192
	ds_write_b64 v83, v[94:95] offset:24576
	v_lshlrev_b32_e32 v92, 16, v114
	v_and_b32_e32 v93, s89, v114
	v_pk_mul_f32 v[92:93], v[92:93], v[86:87]
	ds_write_b64 v83, v[92:93] offset:32768
	v_lshlrev_b32_e32 v92, 16, v99
	v_and_b32_e32 v93, s89, v99
	v_lshlrev_b32_e32 v94, 16, v103
	v_and_b32_e32 v95, s89, v103
	v_pk_fma_f32 v[84:85], v[92:93], s[46:47], v[84:85]
	v_pk_mul_f32 v[94:95], v[94:95], v[86:87]
	ds_write_b64 v83, v[94:95] offset:256
	v_lshlrev_b32_e32 v92, 16, v107
	v_and_b32_e32 v93, s89, v107
	v_exp_f32_e64 v88, -v84
	v_exp_f32_e64 v89, -v85
	v_exp_f32_e32 v90, v84
	v_exp_f32_e32 v91, v85
	v_lshlrev_b32_e32 v94, 16, v111
	v_and_b32_e32 v95, s89, v111
	v_pk_mul_f32 v[92:93], v[92:93], v[90:91]
	v_pk_mul_f32 v[94:95], v[94:95], v[90:91]
	ds_write_b64 v83, v[92:93] offset:8448
	ds_write_b64 v83, v[94:95] offset:24832
	v_lshlrev_b32_e32 v92, 16, v115
	v_and_b32_e32 v93, s89, v115
	v_pk_mul_f32 v[92:93], v[92:93], v[88:89]
	ds_write_b64 v83, v[92:93] offset:33024
	v_lshlrev_b32_e32 v92, 16, v100
	v_and_b32_e32 v93, s89, v100
	v_lshlrev_b32_e32 v94, 16, v104
	v_and_b32_e32 v95, s89, v104
	v_pk_fma_f32 v[84:85], v[92:93], s[46:47], v[84:85]
	v_pk_mul_f32 v[94:95], v[94:95], v[88:89]
	ds_write_b64 v83, v[94:95] offset:512
	v_lshlrev_b32_e32 v92, 16, v108
	v_and_b32_e32 v93, s89, v108
	v_exp_f32_e64 v86, -v84
	v_exp_f32_e64 v87, -v85
	v_exp_f32_e32 v90, v84
	v_exp_f32_e32 v91, v85
	v_lshlrev_b32_e32 v94, 16, v112
	v_and_b32_e32 v95, s89, v112
	v_pk_mul_f32 v[92:93], v[92:93], v[90:91]
	v_pk_mul_f32 v[94:95], v[94:95], v[90:91]
	ds_write_b64 v83, v[92:93] offset:8704
	ds_write_b64 v83, v[94:95] offset:25088
	v_lshlrev_b32_e32 v92, 16, v116
	v_and_b32_e32 v93, s89, v116
	v_pk_mul_f32 v[92:93], v[92:93], v[86:87]
	ds_write_b64 v83, v[92:93] offset:33280
	v_lshlrev_b32_e32 v92, 16, v101
	v_and_b32_e32 v93, s89, v101
	v_lshlrev_b32_e32 v94, 16, v105
	v_and_b32_e32 v95, s89, v105
	v_pk_fma_f32 v[84:85], v[92:93], s[46:47], v[84:85]
	v_pk_mul_f32 v[94:95], v[94:95], v[86:87]
	ds_write_b64 v83, v[94:95] offset:768
	v_lshlrev_b32_e32 v92, 16, v109
	v_and_b32_e32 v93, s89, v109
	v_exp_f32_e64 v88, -v84
	v_exp_f32_e64 v89, -v85
	v_exp_f32_e32 v90, v84
	v_exp_f32_e32 v91, v85
	v_lshlrev_b32_e32 v94, 16, v113
	v_and_b32_e32 v95, s89, v113
	v_pk_mul_f32 v[92:93], v[92:93], v[90:91]
	v_pk_mul_f32 v[94:95], v[94:95], v[90:91]
	ds_write_b64 v83, v[92:93] offset:8960
	ds_write_b64 v83, v[88:89] offset:17152
	ds_write_b64 v83, v[94:95] offset:25344
	v_lshlrev_b32_e32 v92, 16, v117
	v_and_b32_e32 v93, s89, v117
	ds_write_b64 v83, v[92:93] offset:33536
	s_mov_b32 s88, 0x15000
	s_mov_b32 s86, 0
	s_mov_b32 s7, 0
	s_mov_b32 s51, 0
	s_waitcnt lgkmcnt(0)
	s_barrier

.Lld_proc_a:
	s_add_i32 s8, s86, 2
	s_cmp_lt_u32 s8, 0x88
	s_cbranch_scc0 .Lld_noproc_a
	v_add_u32_e32 v83, s88, v7
	v_add_u32_e32 v96, s88, v8
	s_mov_b32 s46, 0x3fb8aa3b
	s_mov_b32 s47, 0x3fb8aa3b
	v_lshlrev_b32_e32 v92, 16, v29
	v_and_b32_e32 v93, s89, v29
	ds_write_b64 v96, v[92:93]
	v_lshlrev_b32_e32 v92, 16, v9
	v_and_b32_e32 v93, s89, v9
	v_lshlrev_b32_e32 v94, 16, v13
	v_and_b32_e32 v95, s89, v13
	v_pk_mul_f32 v[84:85], v[92:93], s[46:47]
	ds_write_b64 v83, v[94:95] offset:0
	v_lshlrev_b32_e32 v92, 16, v17
	v_and_b32_e32 v93, s89, v17
	v_exp_f32_e64 v86, -v84
	v_exp_f32_e64 v87, -v85
	v_exp_f32_e32 v90, v84
	v_exp_f32_e32 v91, v85
	v_lshlrev_b32_e32 v94, 16, v21
	v_and_b32_e32 v95, s89, v21
	v_pk_mul_f32 v[92:93], v[92:93], v[90:91]
	v_pk_mul_f32 v[94:95], v[94:95], v[90:91]
	ds_write_b64 v83, v[92:93] offset:8192
	ds_write_b64 v83, v[94:95] offset:24576
	v_lshlrev_b32_e32 v92, 16, v25
	v_and_b32_e32 v93, s89, v25
	v_pk_mul_f32 v[92:93], v[92:93], v[86:87]
	ds_write_b64 v83, v[92:93] offset:32768
	v_lshlrev_b32_e32 v92, 16, v10
	v_and_b32_e32 v93, s89, v10
	v_lshlrev_b32_e32 v94, 16, v14
	v_and_b32_e32 v95, s89, v14
	v_pk_fma_f32 v[84:85], v[92:93], s[46:47], v[84:85]
	v_pk_mul_f32 v[94:95], v[94:95], v[86:87]
	ds_write_b64 v83, v[94:95] offset:256
	v_lshlrev_b32_e32 v92, 16, v18
	v_and_b32_e32 v93, s89, v18
	v_exp_f32_e64 v88, -v84
	v_exp_f32_e64 v89, -v85
	v_exp_f32_e32 v90, v84
	v_exp_f32_e32 v91, v85
	v_lshlrev_b32_e32 v94, 16, v22
	v_and_b32_e32 v95, s89, v22
	v_pk_mul_f32 v[92:93], v[92:93], v[90:91]
	v_pk_mul_f32 v[94:95], v[94:95], v[90:91]
	ds_write_b64 v83, v[92:93] offset:8448
	ds_write_b64 v83, v[94:95] offset:24832
	v_lshlrev_b32_e32 v92, 16, v26
	v_and_b32_e32 v93, s89, v26
	v_pk_mul_f32 v[92:93], v[92:93], v[88:89]
	ds_write_b64 v83, v[92:93] offset:33024
	v_lshlrev_b32_e32 v92, 16, v11
	v_and_b32_e32 v93, s89, v11
	v_lshlrev_b32_e32 v94, 16, v15
	v_and_b32_e32 v95, s89, v15
	v_pk_fma_f32 v[84:85], v[92:93], s[46:47], v[84:85]
	v_pk_mul_f32 v[94:95], v[94:95], v[88:89]
	ds_write_b64 v83, v[94:95] offset:512
	v_lshlrev_b32_e32 v92, 16, v19
	v_and_b32_e32 v93, s89, v19
	v_exp_f32_e64 v86, -v84
	v_exp_f32_e64 v87, -v85
	v_exp_f32_e32 v90, v84
	v_exp_f32_e32 v91, v85
	v_lshlrev_b32_e32 v94, 16, v23
	v_and_b32_e32 v95, s89, v23
	v_pk_mul_f32 v[92:93], v[92:93], v[90:91]
	v_pk_mul_f32 v[94:95], v[94:95], v[90:91]
	ds_write_b64 v83, v[92:93] offset:8704
	ds_write_b64 v83, v[94:95] offset:25088
	v_lshlrev_b32_e32 v92, 16, v27
	v_and_b32_e32 v93, s89, v27
	v_pk_mul_f32 v[92:93], v[92:93], v[86:87]
	ds_write_b64 v83, v[92:93] offset:33280
	v_lshlrev_b32_e32 v92, 16, v12
	v_and_b32_e32 v93, s89, v12
	v_lshlrev_b32_e32 v94, 16, v16
	v_and_b32_e32 v95, s89, v16
	v_pk_fma_f32 v[84:85], v[92:93], s[46:47], v[84:85]
	v_pk_mul_f32 v[94:95], v[94:95], v[86:87]
	ds_write_b64 v83, v[94:95] offset:768
	v_lshlrev_b32_e32 v92, 16, v20
	v_and_b32_e32 v93, s89, v20
	v_exp_f32_e64 v88, -v84
	v_exp_f32_e64 v89, -v85
	v_exp_f32_e32 v90, v84
	v_exp_f32_e32 v91, v85
	v_lshlrev_b32_e32 v94, 16, v24
	v_and_b32_e32 v95, s89, v24
	v_pk_mul_f32 v[92:93], v[92:93], v[90:91]
	v_pk_mul_f32 v[94:95], v[94:95], v[90:91]
	ds_write_b64 v83, v[92:93] offset:8960
	ds_write_b64 v83, v[88:89] offset:17152
	ds_write_b64 v83, v[94:95] offset:25344
	v_lshlrev_b32_e32 v92, 16, v28
	v_and_b32_e32 v93, s89, v28
	ds_write_b64 v83, v[92:93] offset:33536

.Lld_proc_b:
	s_add_i32 s8, s86, 2
	s_cmp_lt_u32 s8, 0x88
	s_cbranch_scc0 .Lld_noproc_b
	v_add_u32_e32 v83, s88, v7
	v_add_u32_e32 v96, s88, v8
	s_mov_b32 s46, 0x3fb8aa3b
	s_mov_b32 s47, 0x3fb8aa3b
	v_lshlrev_b32_e32 v92, 16, v118
	v_and_b32_e32 v93, s89, v118
	ds_write_b64 v96, v[92:93]
	v_lshlrev_b32_e32 v92, 16, v98
	v_and_b32_e32 v93, s89, v98
	v_lshlrev_b32_e32 v94, 16, v102
	v_and_b32_e32 v95, s89, v102
	v_pk_mul_f32 v[84:85], v[92:93], s[46:47]
	ds_write_b64 v83, v[94:95] offset:0
	v_lshlrev_b32_e32 v92, 16, v106
	v_and_b32_e32 v93, s89, v106
	v_exp_f32_e64 v86, -v84
	v_exp_f32_e64 v87, -v85
	v_exp_f32_e32 v90, v84
	v_exp_f32_e32 v91, v85
	v_lshlrev_b32_e32 v94, 16, v110
	v_and_b32_e32 v95, s89, v110
	v_pk_mul_f32 v[92:93], v[92:93], v[90:91]
	v_pk_mul_f32 v[94:95], v[94:95], v[90:91]
	ds_write_b64 v83, v[92:93] offset:8192
	ds_write_b64 v83, v[94:95] offset:24576
	v_lshlrev_b32_e32 v92, 16, v114
	v_and_b32_e32 v93, s89, v114
	v_pk_mul_f32 v[92:93], v[92:93], v[86:87]
	ds_write_b64 v83, v[92:93] offset:32768
	v_lshlrev_b32_e32 v92, 16, v99
	v_and_b32_e32 v93, s89, v99
	v_lshlrev_b32_e32 v94, 16, v103
	v_and_b32_e32 v95, s89, v103
	v_pk_fma_f32 v[84:85], v[92:93], s[46:47], v[84:85]
	v_pk_mul_f32 v[94:95], v[94:95], v[86:87]
	ds_write_b64 v83, v[94:95] offset:256
	v_lshlrev_b32_e32 v92, 16, v107
	v_and_b32_e32 v93, s89, v107
	v_exp_f32_e64 v88, -v84
	v_exp_f32_e64 v89, -v85
	v_exp_f32_e32 v90, v84
	v_exp_f32_e32 v91, v85
	v_lshlrev_b32_e32 v94, 16, v111
	v_and_b32_e32 v95, s89, v111
	v_pk_mul_f32 v[92:93], v[92:93], v[90:91]
	v_pk_mul_f32 v[94:95], v[94:95], v[90:91]
	ds_write_b64 v83, v[92:93] offset:8448
	ds_write_b64 v83, v[94:95] offset:24832
	v_lshlrev_b32_e32 v92, 16, v115
	v_and_b32_e32 v93, s89, v115
	v_pk_mul_f32 v[92:93], v[92:93], v[88:89]
	ds_write_b64 v83, v[92:93] offset:33024
	v_lshlrev_b32_e32 v92, 16, v100
	v_and_b32_e32 v93, s89, v100
	v_lshlrev_b32_e32 v94, 16, v104
	v_and_b32_e32 v95, s89, v104
	v_pk_fma_f32 v[84:85], v[92:93], s[46:47], v[84:85]
	v_pk_mul_f32 v[94:95], v[94:95], v[88:89]
	ds_write_b64 v83, v[94:95] offset:512
	v_lshlrev_b32_e32 v92, 16, v108
	v_and_b32_e32 v93, s89, v108
	v_exp_f32_e64 v86, -v84
	v_exp_f32_e64 v87, -v85
	v_exp_f32_e32 v90, v84
	v_exp_f32_e32 v91, v85
	v_lshlrev_b32_e32 v94, 16, v112
	v_and_b32_e32 v95, s89, v112
	v_pk_mul_f32 v[92:93], v[92:93], v[90:91]
	v_pk_mul_f32 v[94:95], v[94:95], v[90:91]
	ds_write_b64 v83, v[92:93] offset:8704
	ds_write_b64 v83, v[94:95] offset:25088
	v_lshlrev_b32_e32 v92, 16, v116
	v_and_b32_e32 v93, s89, v116
	v_pk_mul_f32 v[92:93], v[92:93], v[86:87]
	ds_write_b64 v83, v[92:93] offset:33280
	v_lshlrev_b32_e32 v92, 16, v101
	v_and_b32_e32 v93, s89, v101
	v_lshlrev_b32_e32 v94, 16, v105
	v_and_b32_e32 v95, s89, v105
	v_pk_fma_f32 v[84:85], v[92:93], s[46:47], v[84:85]
	v_pk_mul_f32 v[94:95], v[94:95], v[86:87]
	ds_write_b64 v83, v[94:95] offset:768
	v_lshlrev_b32_e32 v92, 16, v109
	v_and_b32_e32 v93, s89, v109
	v_exp_f32_e64 v88, -v84
	v_exp_f32_e64 v89, -v85
	v_exp_f32_e32 v90, v84
	v_exp_f32_e32 v91, v85
	v_lshlrev_b32_e32 v94, 16, v113
	v_and_b32_e32 v95, s89, v113
	v_pk_mul_f32 v[92:93], v[92:93], v[90:91]
	v_pk_mul_f32 v[94:95], v[94:95], v[90:91]
	ds_write_b64 v83, v[92:93] offset:8960
	ds_write_b64 v83, v[88:89] offset:17152
	ds_write_b64 v83, v[94:95] offset:25344
	v_lshlrev_b32_e32 v92, 16, v117
	v_and_b32_e32 v93, s89, v117
	ds_write_b64 v83, v[92:93] offset:33536
